# v4 (sub-group barriers + v2) + residual-GEMM prologue: compiler vmcnt(0) before the accumulator unpack relaxed to vmcnt(6) (the residual tile loads are older than the 6 staging loads)
# baseline (speedup 1.0000x reference)
.LBB0_1069:
	v_or_b32_e32 v1, s10, v139
	s_add_u32 s8, s8, 0x36300000
	v_lshlrev_b32_e32 v67, 6, v1
	s_movk_i32 s16, 0x3c0
	v_lshlrev_b32_e32 v68, 2, v1
	s_addc_u32 s9, s9, 0
	v_and_or_b32 v67, v67, s16, v66
	s_lshl_b32 s16, s28, 13
	v_and_b32_e32 v68, 32, v68
	v_bitop3_b32 v150, v67, s16, v68 bitop3:0xde
	v_lshlrev_b32_e32 v67, 2, v139
	v_lshl_or_b32 v66, v139, 6, v66
	s_lshl_b32 s16, s12, 12
	v_and_b32_e32 v67, 32, v67
	v_bitop3_b32 v146, v66, s16, v67 bitop3:0xde
	s_add_u32 s16, s50, 0x8000
	s_addc_u32 s17, s51, 0
	s_add_i32 m0, s20, 0x18000
	v_lshl_add_u64 v[66:67], s[16:17], 0, v[114:115]
	v_mov_b32_e32 v137, v115
	s_waitcnt vmcnt(2)
	s_barrier
	global_load_lds_dwordx4 v[66:67], off
	s_add_i32 m0, s20, 0x1a000
	v_lshl_add_u64 v[66:67], s[16:17], 0, v[136:137]
	s_add_u32 s16, s52, 0x8000
	v_mov_b32_e32 v133, v115
	s_addc_u32 s17, s53, 0
	s_add_i32 s59, s20, 0x8000
	v_mov_b32_e32 v135, v115
	global_load_lds_dwordx4 v[66:67], off
	v_lshl_add_u64 v[66:67], s[16:17], 0, v[132:133]
	s_mov_b32 m0, s59
	s_add_i32 s60, s20, 0xa000
	global_load_lds_dwordx4 v[66:67], off
	v_lshl_add_u64 v[66:67], s[16:17], 0, v[134:135]
	s_add_u32 s16, s50, 0x9000
	s_mov_b32 m0, s60
	s_addc_u32 s17, s51, 0
	global_load_lds_dwordx4 v[66:67], off
	s_add_i32 m0, s20, 0x1c000
	v_lshl_add_u64 v[66:67], s[16:17], 0, v[114:115]
	global_load_lds_dwordx4 v[66:67], off
	v_lshl_add_u64 v[66:67], s[16:17], 0, v[136:137]
	s_add_i32 m0, s20, 0x1e000
	v_lshlrev_b32_e32 v147, 3, v138
	global_load_lds_dwordx4 v[66:67], off
	s_waitcnt vmcnt(6)
	s_barrier
	s_waitcnt vmcnt(6)
	v_lshlrev_b32_e32 v116, 16, v62
	v_and_b32_e32 v117, 0xffff0000, v62
	v_lshlrev_b32_e32 v118, 16, v63
	v_and_b32_e32 v119, 0xffff0000, v63
	v_lshlrev_b32_e32 v124, 16, v64
	v_and_b32_e32 v125, 0xffff0000, v64
	v_lshlrev_b32_e32 v126, 16, v65
	v_and_b32_e32 v127, 0xffff0000, v65
	v_lshlrev_b32_e32 v120, 16, v58
	v_and_b32_e32 v121, 0xffff0000, v58
	v_lshlrev_b32_e32 v122, 16, v59
	v_and_b32_e32 v123, 0xffff0000, v59
	v_lshlrev_b32_e32 v128, 16, v60
	v_and_b32_e32 v129, 0xffff0000, v60
	v_lshlrev_b32_e32 v130, 16, v61
	v_and_b32_e32 v131, 0xffff0000, v61
	v_lshlrev_b32_e32 v98, 16, v54
	v_and_b32_e32 v99, 0xffff0000, v54
	v_lshlrev_b32_e32 v100, 16, v55
	v_and_b32_e32 v101, 0xffff0000, v55
	v_lshlrev_b32_e32 v102, 16, v56
	v_and_b32_e32 v103, 0xffff0000, v56
	v_lshlrev_b32_e32 v104, 16, v57
	v_and_b32_e32 v105, 0xffff0000, v57
	v_lshlrev_b32_e32 v106, 16, v50
	v_and_b32_e32 v107, 0xffff0000, v50
	v_lshlrev_b32_e32 v108, 16, v51
	v_and_b32_e32 v109, 0xffff0000, v51
	v_lshlrev_b32_e32 v110, 16, v52
	v_and_b32_e32 v111, 0xffff0000, v52
	v_lshlrev_b32_e32 v112, 16, v53
	v_and_b32_e32 v113, 0xffff0000, v53
	v_lshlrev_b32_e32 v82, 16, v46
	v_and_b32_e32 v83, 0xffff0000, v46
	v_lshlrev_b32_e32 v84, 16, v47
	v_and_b32_e32 v85, 0xffff0000, v47
	v_lshlrev_b32_e32 v90, 16, v48
	v_and_b32_e32 v91, 0xffff0000, v48
	v_lshlrev_b32_e32 v92, 16, v49
	v_and_b32_e32 v93, 0xffff0000, v49
	v_lshlrev_b32_e32 v86, 16, v42
	v_and_b32_e32 v87, 0xffff0000, v42
	v_lshlrev_b32_e32 v88, 16, v43
	v_and_b32_e32 v89, 0xffff0000, v43
	v_lshlrev_b32_e32 v94, 16, v44
	v_and_b32_e32 v95, 0xffff0000, v44
	v_lshlrev_b32_e32 v96, 16, v45
	v_and_b32_e32 v97, 0xffff0000, v45
	v_lshlrev_b32_e32 v58, 16, v38
	v_and_b32_e32 v59, 0xffff0000, v38
	v_lshlrev_b32_e32 v60, 16, v39
	v_and_b32_e32 v61, 0xffff0000, v39
	v_lshlrev_b32_e32 v70, 16, v40
	v_and_b32_e32 v71, 0xffff0000, v40
	v_lshlrev_b32_e32 v72, 16, v41
	v_and_b32_e32 v73, 0xffff0000, v41
	v_lshlrev_b32_e32 v74, 16, v30
	v_and_b32_e32 v75, 0xffff0000, v30
	v_lshlrev_b32_e32 v76, 16, v31
	v_and_b32_e32 v77, 0xffff0000, v31
	v_lshlrev_b32_e32 v78, 16, v32
	v_and_b32_e32 v79, 0xffff0000, v32
	v_lshlrev_b32_e32 v80, 16, v33
	v_and_b32_e32 v81, 0xffff0000, v33
	v_lshlrev_b32_e32 v50, 16, v34
	v_and_b32_e32 v51, 0xffff0000, v34
	v_lshlrev_b32_e32 v52, 16, v35
	v_and_b32_e32 v53, 0xffff0000, v35
	v_lshlrev_b32_e32 v62, 16, v36
	v_and_b32_e32 v63, 0xffff0000, v36
	v_lshlrev_b32_e32 v64, 16, v37
	v_and_b32_e32 v65, 0xffff0000, v37
	v_lshlrev_b32_e32 v54, 16, v26
	v_and_b32_e32 v55, 0xffff0000, v26
	v_lshlrev_b32_e32 v56, 16, v27
	v_and_b32_e32 v57, 0xffff0000, v27
	v_lshlrev_b32_e32 v66, 16, v28
	v_and_b32_e32 v67, 0xffff0000, v28
	v_lshlrev_b32_e32 v68, 16, v29
	v_and_b32_e32 v69, 0xffff0000, v29
	v_lshlrev_b32_e32 v34, 16, v22
	v_and_b32_e32 v35, 0xffff0000, v22
	v_lshlrev_b32_e32 v36, 16, v23
	v_and_b32_e32 v37, 0xffff0000, v23
	v_lshlrev_b32_e32 v38, 16, v24
	v_and_b32_e32 v39, 0xffff0000, v24
	v_lshlrev_b32_e32 v40, 16, v25
	v_and_b32_e32 v41, 0xffff0000, v25
	v_lshlrev_b32_e32 v42, 16, v18
	v_and_b32_e32 v43, 0xffff0000, v18
	v_lshlrev_b32_e32 v44, 16, v19
	v_and_b32_e32 v45, 0xffff0000, v19
	v_lshlrev_b32_e32 v46, 16, v20
	v_and_b32_e32 v47, 0xffff0000, v20
	v_lshlrev_b32_e32 v48, 16, v21
	v_and_b32_e32 v49, 0xffff0000, v21
	v_lshlrev_b32_e32 v18, 16, v10
	v_and_b32_e32 v19, 0xffff0000, v10
	v_lshlrev_b32_e32 v20, 16, v11
	v_and_b32_e32 v21, 0xffff0000, v11
	v_lshlrev_b32_e32 v26, 16, v12
	v_and_b32_e32 v27, 0xffff0000, v12
	v_lshlrev_b32_e32 v28, 16, v13
	v_and_b32_e32 v29, 0xffff0000, v13
	v_lshlrev_b32_e32 v22, 16, v2
	v_and_b32_e32 v23, 0xffff0000, v2
	v_lshlrev_b32_e32 v24, 16, v3
	v_and_b32_e32 v25, 0xffff0000, v3
	v_lshlrev_b32_e32 v30, 16, v4
	v_and_b32_e32 v31, 0xffff0000, v4
	v_lshlrev_b32_e32 v32, 16, v5
	v_and_b32_e32 v33, 0xffff0000, v5
	v_lshlrev_b32_e32 v2, 16, v6
	v_and_b32_e32 v3, 0xffff0000, v6
	v_lshlrev_b32_e32 v4, 16, v7
	v_and_b32_e32 v5, 0xffff0000, v7
	v_lshlrev_b32_e32 v6, 16, v8
	v_and_b32_e32 v7, 0xffff0000, v8
	v_lshlrev_b32_e32 v8, 16, v9
	v_and_b32_e32 v9, 0xffff0000, v9
	v_lshlrev_b32_e32 v10, 16, v14
	v_and_b32_e32 v11, 0xffff0000, v14
	v_lshlrev_b32_e32 v12, 16, v15
	v_and_b32_e32 v13, 0xffff0000, v15
	v_lshlrev_b32_e32 v14, 16, v16
	v_and_b32_e32 v15, 0xffff0000, v16
	v_lshlrev_b32_e32 v16, 16, v17
	v_and_b32_e32 v17, 0xffff0000, v17
	v_mov_b32_e32 v149, s11
	v_or_b32_e32 v148, s10, v139
	v_cmp_eq_u32_e64 s[38:39], 0, v138
	v_lshlrev_b64 v[138:139], 7, v[148:149]
	v_lshlrev_b32_e32 v148, 1, v147
	v_lshlrev_b32_e32 v147, 10, v140
	v_and_b32_e32 v147, 0xfffff800, v147
	v_lshl_add_u32 v141, v141, 7, v147
	v_and_b32_e32 v140, 1, v140
	v_lshl_or_b32 v140, v140, 6, v141
	v_lshl_add_u32 v140, v142, 1, v140
	v_lshlrev_b32_e32 v142, 10, v143
	v_and_b32_e32 v142, 0xfffff800, v142
	v_lshl_add_u32 v142, v144, 7, v142
	v_and_b32_e32 v143, 1, v143
	s_cmpk_lt_u32 s24, 0x100
	v_lshl_add_u64 v[138:139], s[26:27], 0, v[138:139]
	v_mov_b32_e32 v149, v115
	v_lshl_or_b32 v142, v143, 6, v142
	s_cselect_b64 s[10:11], -1, 0
	s_mov_b32 s61, 0
	s_ashr_i32 s62, s7, 31
	v_lshl_add_u64 v[138:139], v[138:139], 0, v[148:149]
	v_mov_b32_e32 v141, v115
	v_lshl_add_u32 v142, v145, 1, v142
	v_mov_b32_e32 v143, v115
	v_add_u32_e32 v147, 0, v150
	s_branch .LBB0_1072

.LBB0_1324:
	v_or_b32_e32 v1, s10, v139
	s_add_u32 s8, s8, 0x36300000
	v_lshlrev_b32_e32 v67, 6, v1
	s_movk_i32 s16, 0x3c0
	v_lshlrev_b32_e32 v68, 2, v1
	s_addc_u32 s9, s9, 0
	v_and_or_b32 v67, v67, s16, v66
	s_lshl_b32 s16, s26, 13
	v_and_b32_e32 v68, 32, v68
	v_bitop3_b32 v150, v67, s16, v68 bitop3:0xde
	v_lshlrev_b32_e32 v67, 2, v139
	v_lshl_or_b32 v66, v139, 6, v66
	s_lshl_b32 s16, s14, 12
	v_and_b32_e32 v67, 32, v67
	v_bitop3_b32 v146, v66, s16, v67 bitop3:0xde
	s_add_u32 s16, s50, 0x8000
	s_addc_u32 s17, s51, 0
	s_add_i32 m0, s37, 0x18000
	v_lshl_add_u64 v[66:67], s[16:17], 0, v[114:115]
	v_mov_b32_e32 v137, v115
	s_waitcnt vmcnt(2)
	s_barrier
	global_load_lds_dwordx4 v[66:67], off
	s_add_i32 m0, s37, 0x1a000
	v_lshl_add_u64 v[66:67], s[16:17], 0, v[136:137]
	s_add_u32 s16, s52, 0x8000
	v_mov_b32_e32 v133, v115
	s_addc_u32 s17, s53, 0
	s_add_i32 s61, s37, 0x8000
	v_mov_b32_e32 v135, v115
	global_load_lds_dwordx4 v[66:67], off
	v_lshl_add_u64 v[66:67], s[16:17], 0, v[132:133]
	s_mov_b32 m0, s61
	s_add_i32 s62, s37, 0xa000
	global_load_lds_dwordx4 v[66:67], off
	v_lshl_add_u64 v[66:67], s[16:17], 0, v[134:135]
	s_add_u32 s16, s50, 0x9000
	s_mov_b32 m0, s62
	s_addc_u32 s17, s51, 0
	global_load_lds_dwordx4 v[66:67], off
	s_add_i32 m0, s37, 0x1c000
	v_lshl_add_u64 v[66:67], s[16:17], 0, v[114:115]
	global_load_lds_dwordx4 v[66:67], off
	v_lshl_add_u64 v[66:67], s[16:17], 0, v[136:137]
	s_add_i32 m0, s37, 0x1e000
	v_lshlrev_b32_e32 v147, 3, v138
	global_load_lds_dwordx4 v[66:67], off
	s_waitcnt vmcnt(6)
	s_barrier
	s_waitcnt vmcnt(6)
	v_lshlrev_b32_e32 v116, 16, v62
	v_and_b32_e32 v117, 0xffff0000, v62
	v_lshlrev_b32_e32 v118, 16, v63
	v_and_b32_e32 v119, 0xffff0000, v63
	v_lshlrev_b32_e32 v124, 16, v64
	v_and_b32_e32 v125, 0xffff0000, v64
	v_lshlrev_b32_e32 v126, 16, v65
	v_and_b32_e32 v127, 0xffff0000, v65
	v_lshlrev_b32_e32 v120, 16, v58
	v_and_b32_e32 v121, 0xffff0000, v58
	v_lshlrev_b32_e32 v122, 16, v59
	v_and_b32_e32 v123, 0xffff0000, v59
	v_lshlrev_b32_e32 v128, 16, v60
	v_and_b32_e32 v129, 0xffff0000, v60
	v_lshlrev_b32_e32 v130, 16, v61
	v_and_b32_e32 v131, 0xffff0000, v61
	v_lshlrev_b32_e32 v98, 16, v54
	v_and_b32_e32 v99, 0xffff0000, v54
	v_lshlrev_b32_e32 v100, 16, v55
	v_and_b32_e32 v101, 0xffff0000, v55
	v_lshlrev_b32_e32 v102, 16, v56
	v_and_b32_e32 v103, 0xffff0000, v56
	v_lshlrev_b32_e32 v104, 16, v57
	v_and_b32_e32 v105, 0xffff0000, v57
	v_lshlrev_b32_e32 v106, 16, v50
	v_and_b32_e32 v107, 0xffff0000, v50
	v_lshlrev_b32_e32 v108, 16, v51
	v_and_b32_e32 v109, 0xffff0000, v51
	v_lshlrev_b32_e32 v110, 16, v52
	v_and_b32_e32 v111, 0xffff0000, v52
	v_lshlrev_b32_e32 v112, 16, v53
	v_and_b32_e32 v113, 0xffff0000, v53
	v_lshlrev_b32_e32 v82, 16, v46
	v_and_b32_e32 v83, 0xffff0000, v46
	v_lshlrev_b32_e32 v84, 16, v47
	v_and_b32_e32 v85, 0xffff0000, v47
	v_lshlrev_b32_e32 v90, 16, v48
	v_and_b32_e32 v91, 0xffff0000, v48
	v_lshlrev_b32_e32 v92, 16, v49
	v_and_b32_e32 v93, 0xffff0000, v49
	v_lshlrev_b32_e32 v86, 16, v42
	v_and_b32_e32 v87, 0xffff0000, v42
	v_lshlrev_b32_e32 v88, 16, v43
	v_and_b32_e32 v89, 0xffff0000, v43
	v_lshlrev_b32_e32 v94, 16, v44
	v_and_b32_e32 v95, 0xffff0000, v44
	v_lshlrev_b32_e32 v96, 16, v45
	v_and_b32_e32 v97, 0xffff0000, v45
	v_lshlrev_b32_e32 v58, 16, v38
	v_and_b32_e32 v59, 0xffff0000, v38
	v_lshlrev_b32_e32 v60, 16, v39
	v_and_b32_e32 v61, 0xffff0000, v39
	v_lshlrev_b32_e32 v70, 16, v40
	v_and_b32_e32 v71, 0xffff0000, v40
	v_lshlrev_b32_e32 v72, 16, v41
	v_and_b32_e32 v73, 0xffff0000, v41
	v_lshlrev_b32_e32 v74, 16, v30
	v_and_b32_e32 v75, 0xffff0000, v30
	v_lshlrev_b32_e32 v76, 16, v31
	v_and_b32_e32 v77, 0xffff0000, v31
	v_lshlrev_b32_e32 v78, 16, v32
	v_and_b32_e32 v79, 0xffff0000, v32
	v_lshlrev_b32_e32 v80, 16, v33
	v_and_b32_e32 v81, 0xffff0000, v33
	v_lshlrev_b32_e32 v50, 16, v34
	v_and_b32_e32 v51, 0xffff0000, v34
	v_lshlrev_b32_e32 v52, 16, v35
	v_and_b32_e32 v53, 0xffff0000, v35
	v_lshlrev_b32_e32 v62, 16, v36
	v_and_b32_e32 v63, 0xffff0000, v36
	v_lshlrev_b32_e32 v64, 16, v37
	v_and_b32_e32 v65, 0xffff0000, v37
	v_lshlrev_b32_e32 v54, 16, v26
	v_and_b32_e32 v55, 0xffff0000, v26
	v_lshlrev_b32_e32 v56, 16, v27
	v_and_b32_e32 v57, 0xffff0000, v27
	v_lshlrev_b32_e32 v66, 16, v28
	v_and_b32_e32 v67, 0xffff0000, v28
	v_lshlrev_b32_e32 v68, 16, v29
	v_and_b32_e32 v69, 0xffff0000, v29
	v_lshlrev_b32_e32 v34, 16, v22
	v_and_b32_e32 v35, 0xffff0000, v22
	v_lshlrev_b32_e32 v36, 16, v23
	v_and_b32_e32 v37, 0xffff0000, v23
	v_lshlrev_b32_e32 v38, 16, v24
	v_and_b32_e32 v39, 0xffff0000, v24
	v_lshlrev_b32_e32 v40, 16, v25
	v_and_b32_e32 v41, 0xffff0000, v25
	v_lshlrev_b32_e32 v42, 16, v18
	v_and_b32_e32 v43, 0xffff0000, v18
	v_lshlrev_b32_e32 v44, 16, v19
	v_and_b32_e32 v45, 0xffff0000, v19
	v_lshlrev_b32_e32 v46, 16, v20
	v_and_b32_e32 v47, 0xffff0000, v20
	v_lshlrev_b32_e32 v48, 16, v21
	v_and_b32_e32 v49, 0xffff0000, v21
	v_lshlrev_b32_e32 v18, 16, v10
	v_and_b32_e32 v19, 0xffff0000, v10
	v_lshlrev_b32_e32 v20, 16, v11
	v_and_b32_e32 v21, 0xffff0000, v11
	v_lshlrev_b32_e32 v26, 16, v12
	v_and_b32_e32 v27, 0xffff0000, v12
	v_lshlrev_b32_e32 v28, 16, v13
	v_and_b32_e32 v29, 0xffff0000, v13
	v_lshlrev_b32_e32 v22, 16, v2
	v_and_b32_e32 v23, 0xffff0000, v2
	v_lshlrev_b32_e32 v24, 16, v3
	v_and_b32_e32 v25, 0xffff0000, v3
	v_lshlrev_b32_e32 v30, 16, v4
	v_and_b32_e32 v31, 0xffff0000, v4
	v_lshlrev_b32_e32 v32, 16, v5
	v_and_b32_e32 v33, 0xffff0000, v5
	v_lshlrev_b32_e32 v2, 16, v6
	v_and_b32_e32 v3, 0xffff0000, v6
	v_lshlrev_b32_e32 v4, 16, v7
	v_and_b32_e32 v5, 0xffff0000, v7
	v_lshlrev_b32_e32 v6, 16, v8
	v_and_b32_e32 v7, 0xffff0000, v8
	v_lshlrev_b32_e32 v8, 16, v9
	v_and_b32_e32 v9, 0xffff0000, v9
	v_lshlrev_b32_e32 v10, 16, v14
	v_and_b32_e32 v11, 0xffff0000, v14
	v_lshlrev_b32_e32 v12, 16, v15
	v_and_b32_e32 v13, 0xffff0000, v15
	v_lshlrev_b32_e32 v14, 16, v16
	v_and_b32_e32 v15, 0xffff0000, v16
	v_lshlrev_b32_e32 v16, 16, v17
	v_and_b32_e32 v17, 0xffff0000, v17
	v_mov_b32_e32 v149, s11
	v_or_b32_e32 v148, s10, v139
	v_cmp_eq_u32_e64 s[38:39], 0, v138
	v_lshlrev_b64 v[138:139], 7, v[148:149]
	v_lshlrev_b32_e32 v148, 1, v147
	v_lshlrev_b32_e32 v147, 10, v140
	v_and_b32_e32 v147, 0xfffff800, v147
	v_lshl_add_u32 v141, v141, 7, v147
	v_and_b32_e32 v140, 1, v140
	v_lshl_or_b32 v140, v140, 6, v141
	v_lshl_add_u32 v140, v142, 1, v140
	v_lshlrev_b32_e32 v142, 10, v143
	v_and_b32_e32 v142, 0xfffff800, v142
	v_lshl_add_u32 v142, v144, 7, v142
	v_and_b32_e32 v143, 1, v143
	s_cmpk_lt_u32 s24, 0x100
	v_lshl_add_u64 v[138:139], s[0:1], 0, v[138:139]
	v_mov_b32_e32 v149, v115
	v_lshl_or_b32 v142, v143, 6, v142
	s_cselect_b64 s[10:11], -1, 0
	s_mov_b32 s63, 0
	s_ashr_i32 s64, s7, 31
	v_lshl_add_u64 v[138:139], v[138:139], 0, v[148:149]
	v_mov_b32_e32 v141, v115
	v_lshl_add_u32 v142, v145, 1, v142
	v_mov_b32_e32 v143, v115
	v_add_u32_e32 v147, 0, v150
	s_branch .LBB0_1327

.LBB0_1366:
	v_or_b32_e32 v1, s9, v140
	v_lshlrev_b32_e32 v2, 6, v1
	s_movk_i32 s16, 0x3c0
	v_lshlrev_b32_e32 v3, 2, v1
	v_and_or_b32 v2, v2, s16, v114
	s_lshl_b32 s11, s11, 13
	v_and_b32_e32 v3, 32, v3
	s_ashr_i32 s27, s28, 2
	v_bitop3_b32 v151, v2, s11, v3 bitop3:0xde
	s_lshl_b32 s11, s15, 12
	v_lshlrev_b32_e32 v3, 2, v140
	s_add_u32 s16, s42, 0x8000
	v_mov_b32_e32 v135, v115
	v_lshl_or_b32 v2, v140, 6, v114
	v_and_b32_e32 v3, 32, v3
	s_addc_u32 s17, s43, 0
	v_bitop3_b32 v144, v2, s11, v3 bitop3:0xde
	s_add_i32 m0, s37, 0x18000
	v_lshl_add_u64 v[2:3], s[16:17], 0, v[134:135]
	v_mov_b32_e32 v139, v115
	s_waitcnt vmcnt(2)
	s_barrier
	global_load_lds_dwordx4 v[2:3], off
	s_add_i32 m0, s37, 0x1a000
	v_lshl_add_u64 v[2:3], s[16:17], 0, v[138:139]
	s_add_u32 s16, s44, 0x8000
	v_mov_b32_e32 v133, v115
	s_addc_u32 s17, s45, 0
	s_add_i32 s53, s37, 0x8000
	v_mov_b32_e32 v137, v115
	global_load_lds_dwordx4 v[2:3], off
	v_lshl_add_u64 v[2:3], s[16:17], 0, v[132:133]
	s_mov_b32 m0, s53
	s_add_i32 s54, s37, 0xa000
	global_load_lds_dwordx4 v[2:3], off
	v_lshl_add_u64 v[2:3], s[16:17], 0, v[136:137]
	s_add_u32 s16, s42, 0x9000
	s_mov_b32 m0, s54
	s_addc_u32 s17, s43, 0
	global_load_lds_dwordx4 v[2:3], off
	s_add_i32 m0, s37, 0x1c000
	v_lshl_add_u64 v[2:3], s[16:17], 0, v[134:135]
	global_load_lds_dwordx4 v[2:3], off
	v_lshl_add_u64 v[2:3], s[16:17], 0, v[138:139]
	s_add_i32 m0, s37, 0x1e000
	s_nop 0
	global_load_lds_dwordx4 v[2:3], off
	s_waitcnt vmcnt(6)
	s_barrier
	s_waitcnt vmcnt(6)
	v_lshlrev_b32_e32 v2, 16, v6
	v_and_b32_e32 v3, 0xffff0000, v6
	v_lshlrev_b32_e32 v4, 16, v7
	v_and_b32_e32 v5, 0xffff0000, v7
	v_lshlrev_b32_e32 v6, 16, v8
	v_and_b32_e32 v7, 0xffff0000, v8
	v_lshlrev_b32_e32 v8, 16, v9
	v_and_b32_e32 v9, 0xffff0000, v9
	v_lshlrev_b32_e32 v18, 16, v10
	v_and_b32_e32 v19, 0xffff0000, v10
	v_lshlrev_b32_e32 v20, 16, v11
	v_and_b32_e32 v21, 0xffff0000, v11
	v_lshlrev_b32_e32 v22, 16, v12
	v_and_b32_e32 v23, 0xffff0000, v12
	v_lshlrev_b32_e32 v24, 16, v13
	v_and_b32_e32 v25, 0xffff0000, v13
	v_lshlrev_b32_e32 v10, 16, v14
	v_and_b32_e32 v11, 0xffff0000, v14
	v_lshlrev_b32_e32 v12, 16, v15
	v_and_b32_e32 v13, 0xffff0000, v15
	v_lshlrev_b32_e32 v14, 16, v16
	v_and_b32_e32 v15, 0xffff0000, v16
	v_lshlrev_b32_e32 v16, 16, v17
	v_and_b32_e32 v17, 0xffff0000, v17
	v_lshlrev_b32_e32 v34, 16, v26
	v_and_b32_e32 v35, 0xffff0000, v26
	v_lshlrev_b32_e32 v36, 16, v27
	v_and_b32_e32 v37, 0xffff0000, v27
	v_lshlrev_b32_e32 v38, 16, v28
	v_and_b32_e32 v39, 0xffff0000, v28
	v_lshlrev_b32_e32 v40, 16, v29
	v_and_b32_e32 v41, 0xffff0000, v29
	v_lshlrev_b32_e32 v26, 16, v30
	v_and_b32_e32 v27, 0xffff0000, v30
	v_lshlrev_b32_e32 v28, 16, v31
	v_and_b32_e32 v29, 0xffff0000, v31
	v_lshlrev_b32_e32 v30, 16, v32
	v_and_b32_e32 v31, 0xffff0000, v32
	v_lshlrev_b32_e32 v32, 16, v33
	v_and_b32_e32 v33, 0xffff0000, v33
	v_lshlrev_b32_e32 v50, 16, v42
	v_and_b32_e32 v51, 0xffff0000, v42
	v_lshlrev_b32_e32 v52, 16, v43
	v_and_b32_e32 v53, 0xffff0000, v43
	v_lshlrev_b32_e32 v54, 16, v44
	v_and_b32_e32 v55, 0xffff0000, v44
	v_lshlrev_b32_e32 v56, 16, v45
	v_and_b32_e32 v57, 0xffff0000, v45
	v_lshlrev_b32_e32 v42, 16, v46
	v_and_b32_e32 v43, 0xffff0000, v46
	v_lshlrev_b32_e32 v44, 16, v47
	v_and_b32_e32 v45, 0xffff0000, v47
	v_lshlrev_b32_e32 v46, 16, v48
	v_and_b32_e32 v47, 0xffff0000, v48
	v_lshlrev_b32_e32 v48, 16, v49
	v_and_b32_e32 v49, 0xffff0000, v49
	v_lshlrev_b32_e32 v58, 16, v62
	v_and_b32_e32 v59, 0xffff0000, v62
	v_lshlrev_b32_e32 v60, 16, v63
	v_and_b32_e32 v61, 0xffff0000, v63
	v_lshlrev_b32_e32 v62, 16, v64
	v_and_b32_e32 v63, 0xffff0000, v64
	v_lshlrev_b32_e32 v64, 16, v65
	v_and_b32_e32 v65, 0xffff0000, v65
	v_lshlrev_b32_e32 v66, 16, v70
	v_and_b32_e32 v67, 0xffff0000, v70
	v_lshlrev_b32_e32 v68, 16, v71
	v_and_b32_e32 v69, 0xffff0000, v71
	v_lshlrev_b32_e32 v70, 16, v72
	v_and_b32_e32 v71, 0xffff0000, v72
	v_lshlrev_b32_e32 v72, 16, v73
	v_and_b32_e32 v73, 0xffff0000, v73
	v_lshlrev_b32_e32 v82, 16, v74
	v_and_b32_e32 v83, 0xffff0000, v74
	v_lshlrev_b32_e32 v84, 16, v75
	v_and_b32_e32 v85, 0xffff0000, v75
	v_lshlrev_b32_e32 v90, 16, v76
	v_and_b32_e32 v91, 0xffff0000, v76
	v_lshlrev_b32_e32 v92, 16, v77
	v_and_b32_e32 v93, 0xffff0000, v77
	v_lshlrev_b32_e32 v74, 16, v78
	v_and_b32_e32 v75, 0xffff0000, v78
	v_lshlrev_b32_e32 v76, 16, v79
	v_and_b32_e32 v77, 0xffff0000, v79
	v_lshlrev_b32_e32 v78, 16, v80
	v_and_b32_e32 v79, 0xffff0000, v80
	v_lshlrev_b32_e32 v80, 16, v81
	v_and_b32_e32 v81, 0xffff0000, v81
	v_lshlrev_b32_e32 v98, 16, v86
	v_and_b32_e32 v99, 0xffff0000, v86
	v_lshlrev_b32_e32 v100, 16, v87
	v_and_b32_e32 v101, 0xffff0000, v87
	v_lshlrev_b32_e32 v106, 16, v88
	v_and_b32_e32 v107, 0xffff0000, v88
	v_lshlrev_b32_e32 v108, 16, v89
	v_and_b32_e32 v109, 0xffff0000, v89
	v_lshlrev_b32_e32 v86, 16, v94
	v_and_b32_e32 v87, 0xffff0000, v94
	v_lshlrev_b32_e32 v88, 16, v95
	v_and_b32_e32 v89, 0xffff0000, v95
	v_lshlrev_b32_e32 v94, 16, v96
	v_and_b32_e32 v95, 0xffff0000, v96
	v_lshlrev_b32_e32 v96, 16, v97
	v_and_b32_e32 v97, 0xffff0000, v97
	v_lshlrev_b32_e32 v116, 16, v102
	v_and_b32_e32 v117, 0xffff0000, v102
	v_lshlrev_b32_e32 v118, 16, v103
	v_and_b32_e32 v119, 0xffff0000, v103
	v_lshlrev_b32_e32 v120, 16, v104
	v_and_b32_e32 v121, 0xffff0000, v104
	v_lshlrev_b32_e32 v122, 16, v105
	v_and_b32_e32 v123, 0xffff0000, v105
	v_lshlrev_b32_e32 v102, 16, v110
	v_and_b32_e32 v103, 0xffff0000, v110
	v_lshlrev_b32_e32 v104, 16, v111
	v_and_b32_e32 v105, 0xffff0000, v111
	v_lshlrev_b32_e32 v110, 16, v112
	v_and_b32_e32 v111, 0xffff0000, v112
	v_lshlrev_b32_e32 v112, 16, v113
	v_and_b32_e32 v113, 0xffff0000, v113
	v_lshlrev_b32_e32 v124, 16, v128
	v_and_b32_e32 v125, 0xffff0000, v128
	v_lshlrev_b32_e32 v126, 16, v129
	v_and_b32_e32 v127, 0xffff0000, v129
	v_lshlrev_b32_e32 v128, 16, v130
	v_and_b32_e32 v129, 0xffff0000, v130
	v_lshlrev_b32_e32 v130, 16, v131
	v_and_b32_e32 v131, 0xffff0000, v131
	v_mov_b32_e32 v141, s10
	v_or_b32_e32 v140, s9, v140
	v_lshlrev_b64 v[140:141], 7, v[140:141]
	v_lshl_add_u64 v[140:141], s[0:1], 0, v[140:141]
	v_lshl_add_u64 v[140:141], v[140:141], 0, v[114:115]
	v_lshlrev_b32_e32 v114, 10, v143
	v_and_b32_e32 v114, 0xfffff800, v114
	v_lshl_or_b32 v145, s15, 6, v142
	v_lshl_add_u32 v114, v146, 7, v114
	v_and_b32_e32 v142, 1, v143
	v_lshl_or_b32 v114, v142, 6, v114
	v_lshlrev_b32_e32 v142, 10, v148
	v_and_b32_e32 v142, 0xfffff800, v142
	v_lshl_add_u32 v142, v149, 7, v142
	v_and_b32_e32 v143, 1, v148
	s_cmpk_lt_u32 s8, 0x100
	v_lshl_or_b32 v142, v143, 6, v142
	s_cselect_b64 s[8:9], -1, 0
	v_lshl_add_u32 v114, v147, 1, v114
	v_lshl_add_u32 v142, v150, 1, v142
	v_mov_b32_e32 v143, v115
	s_mov_b32 s55, 0
	v_add_u32_e32 v146, 0, v151
	s_branch .LBB0_1369
